# SwiGLU epilogue with one reciprocal per element and no exponent clamp (as the baseline's math), 72 issue slots per 8 outputs; plus the stacked trims of the previous version
# speedup vs baseline: 1.0431x; 1.0040x over previous
.LBB0_862:
	s_lshl_b32 s0, s68, 7
	s_mov_b32 s69, 0x48000000
	v_lshl_add_u32 v6, s6, 8, v167
	s_and_b32 s0, s0, 0x380
	v_or_b32_e32 v48, s0, v171
	s_nop 15
	s_nop 15
	s_mov_b32 s0, 0x20000
	v_mul_f32_e32 v24, 0xbab8aa3b, v158
	v_mul_f32_e32 v25, 0xbab8aa3b, v159
	v_mul_f32_e32 v26, 0xbab8aa3b, v160
	v_mul_f32_e32 v27, 0xbab8aa3b, v161
	v_mul_f32_e32 v28, 0xbab8aa3b, v150
	v_mul_f32_e32 v29, 0xbab8aa3b, v151
	v_mul_f32_e32 v30, 0xbab8aa3b, v152
	v_mul_f32_e32 v31, 0xbab8aa3b, v153
	v_exp_f32_e32 v24, v24
	v_exp_f32_e32 v25, v25
	v_exp_f32_e32 v26, v26
	v_exp_f32_e32 v27, v27
	v_exp_f32_e32 v28, v28
	v_exp_f32_e32 v29, v29
	v_exp_f32_e32 v30, v30
	v_exp_f32_e32 v31, v31
	v_mul_f32_e32 v8, v158, v154
	v_mul_f32_e32 v9, v159, v155
	v_mul_f32_e32 v10, v160, v156
	v_mul_f32_e32 v11, v161, v157
	v_mul_f32_e32 v12, v150, v146
	v_mul_f32_e32 v13, v151, v147
	v_mul_f32_e32 v14, v152, v148
	v_mul_f32_e32 v15, v153, v149
	v_fma_f32 v24, v24, s69, s69
	v_fma_f32 v25, v25, s69, s69
	v_fma_f32 v26, v26, s69, s69
	v_fma_f32 v27, v27, s69, s69
	v_fma_f32 v28, v28, s69, s69
	v_fma_f32 v29, v29, s69, s69
	v_fma_f32 v30, v30, s69, s69
	v_fma_f32 v31, v31, s69, s69
	v_rcp_f32_e32 v24, v24
	v_rcp_f32_e32 v25, v25
	v_rcp_f32_e32 v26, v26
	v_rcp_f32_e32 v27, v27
	v_rcp_f32_e32 v28, v28
	v_rcp_f32_e32 v29, v29
	v_rcp_f32_e32 v30, v30
	v_rcp_f32_e32 v31, v31
	v_mul_f32_e32 v8, v8, v24
	v_mul_f32_e32 v9, v9, v25
	v_mul_f32_e32 v10, v10, v26
	v_mul_f32_e32 v11, v11, v27
	v_mul_f32_e32 v12, v12, v28
	v_mul_f32_e32 v13, v13, v29
	v_mul_f32_e32 v14, v14, v30
	v_mul_f32_e32 v15, v15, v31
	v_med3_f32 v8, v8, s11, v232
	v_med3_f32 v9, v9, s11, v232
	v_med3_f32 v10, v10, s11, v232
	v_med3_f32 v11, v11, s11, v232
	v_med3_f32 v12, v12, s11, v232
	v_med3_f32 v13, v13, s11, v232
	v_med3_f32 v14, v14, s11, v232
	v_med3_f32 v15, v15, s11, v232
	v_mul_f32_e32 v24, 0xbab8aa3b, v142
	v_mul_f32_e32 v25, 0xbab8aa3b, v143
	v_mul_f32_e32 v26, 0xbab8aa3b, v144
	v_mul_f32_e32 v27, 0xbab8aa3b, v145
	v_mul_f32_e32 v28, 0xbab8aa3b, v134
	v_mul_f32_e32 v29, 0xbab8aa3b, v135
	v_mul_f32_e32 v30, 0xbab8aa3b, v136
	v_mul_f32_e32 v31, 0xbab8aa3b, v137
	v_exp_f32_e32 v24, v24
	v_exp_f32_e32 v25, v25
	v_exp_f32_e32 v26, v26
	v_exp_f32_e32 v27, v27
	v_exp_f32_e32 v28, v28
	v_exp_f32_e32 v29, v29
	v_exp_f32_e32 v30, v30
	v_exp_f32_e32 v31, v31
	v_mul_f32_e32 v16, v142, v138
	v_mul_f32_e32 v17, v143, v139
	v_mul_f32_e32 v18, v144, v140
	v_mul_f32_e32 v19, v145, v141
	v_mul_f32_e32 v20, v134, v130
	v_mul_f32_e32 v21, v135, v131
	v_mul_f32_e32 v22, v136, v132
	v_mul_f32_e32 v23, v137, v133
	v_fma_f32 v24, v24, s69, s69
	v_fma_f32 v25, v25, s69, s69
	v_fma_f32 v26, v26, s69, s69
	v_fma_f32 v27, v27, s69, s69
	v_fma_f32 v28, v28, s69, s69
	v_fma_f32 v29, v29, s69, s69
	v_fma_f32 v30, v30, s69, s69
	v_fma_f32 v31, v31, s69, s69
	v_rcp_f32_e32 v24, v24
	v_rcp_f32_e32 v25, v25
	v_rcp_f32_e32 v26, v26
	v_rcp_f32_e32 v27, v27
	v_rcp_f32_e32 v28, v28
	v_rcp_f32_e32 v29, v29
	v_rcp_f32_e32 v30, v30
	v_rcp_f32_e32 v31, v31
	v_mul_f32_e32 v16, v16, v24
	v_mul_f32_e32 v17, v17, v25
	v_mul_f32_e32 v18, v18, v26
	v_mul_f32_e32 v19, v19, v27
	v_mul_f32_e32 v20, v20, v28
	v_mul_f32_e32 v21, v21, v29
	v_mul_f32_e32 v22, v22, v30
	v_mul_f32_e32 v23, v23, v31
	v_med3_f32 v16, v16, s11, v232
	v_med3_f32 v17, v17, s11, v232
	v_med3_f32 v18, v18, s11, v232
	v_med3_f32 v19, v19, s11, v232
	v_med3_f32 v20, v20, s11, v232
	v_med3_f32 v21, v21, s11, v232
	v_med3_f32 v22, v22, s11, v232
	v_med3_f32 v23, v23, s11, v232
	v_cvt_pk_fp8_f32 v0, v8, v9
	v_cvt_pk_fp8_f32 v1, v12, v13
	v_cvt_pk_fp8_f32 v2, v16, v17
	v_cvt_pk_fp8_f32 v3, v20, v21
	v_cvt_pk_fp8_f32 v0, v10, v11 op_sel:[0,0,1]
	v_cvt_pk_fp8_f32 v1, v14, v15 op_sel:[0,0,1]
	v_cvt_pk_fp8_f32 v2, v18, v19 op_sel:[0,0,1]
	v_cvt_pk_fp8_f32 v3, v22, v23 op_sel:[0,0,1]
	v_ashrrev_i32_e32 v7, 31, v6
	v_lshlrev_b64 v[4:5], 10, v[6:7]
	v_lshl_add_u64 v[4:5], s[58:59], 0, v[4:5]
	v_lshl_add_u64 v[4:5], v[4:5], 0, v[48:49]
	s_nop 1
	v_permlane16_swap_b32_e32 v0, v2
	v_permlane16_swap_b32_e32 v1, v3
	global_store_dwordx4 v[4:5], v[0:3], off
	v_mov_b32_e32 v130, 0
	v_mov_b32_e32 v131, 0
	v_mov_b32_e32 v132, 0
	v_mov_b32_e32 v133, 0
	v_mov_b32_e32 v134, 0
	v_mov_b32_e32 v135, 0
	v_mov_b32_e32 v136, 0
	v_mov_b32_e32 v137, 0
	v_mov_b32_e32 v138, 0
	v_mov_b32_e32 v139, 0
	v_mov_b32_e32 v140, 0
	v_mov_b32_e32 v141, 0
	v_mov_b32_e32 v142, 0
	v_mov_b32_e32 v143, 0
	v_mov_b32_e32 v144, 0
	v_mov_b32_e32 v145, 0
	v_mov_b32_e32 v146, 0
	v_mov_b32_e32 v147, 0
	v_mov_b32_e32 v148, 0
	v_mov_b32_e32 v149, 0
	v_mov_b32_e32 v150, 0
	v_mov_b32_e32 v151, 0
	v_mov_b32_e32 v152, 0
	v_mov_b32_e32 v153, 0
	v_mov_b32_e32 v154, 0
	v_mov_b32_e32 v155, 0
	v_mov_b32_e32 v156, 0
	v_mov_b32_e32 v157, 0
	v_mov_b32_e32 v158, 0
	v_mov_b32_e32 v159, 0
	v_mov_b32_e32 v160, 0
	v_mov_b32_e32 v161, 0
	v_or_b32_e32 v6, 32, v6
	v_mul_f32_e32 v24, 0xbab8aa3b, v126
	v_mul_f32_e32 v25, 0xbab8aa3b, v127
	v_mul_f32_e32 v26, 0xbab8aa3b, v128
	v_mul_f32_e32 v27, 0xbab8aa3b, v129
	v_mul_f32_e32 v28, 0xbab8aa3b, v118
	v_mul_f32_e32 v29, 0xbab8aa3b, v119
	v_mul_f32_e32 v30, 0xbab8aa3b, v120
	v_mul_f32_e32 v31, 0xbab8aa3b, v121
	v_exp_f32_e32 v24, v24
	v_exp_f32_e32 v25, v25
	v_exp_f32_e32 v26, v26
	v_exp_f32_e32 v27, v27
	v_exp_f32_e32 v28, v28
	v_exp_f32_e32 v29, v29
	v_exp_f32_e32 v30, v30
	v_exp_f32_e32 v31, v31
	v_mul_f32_e32 v8, v126, v122
	v_mul_f32_e32 v9, v127, v123
	v_mul_f32_e32 v10, v128, v124
	v_mul_f32_e32 v11, v129, v125
	v_mul_f32_e32 v12, v118, v114
	v_mul_f32_e32 v13, v119, v115
	v_mul_f32_e32 v14, v120, v116
	v_mul_f32_e32 v15, v121, v117
	v_fma_f32 v24, v24, s69, s69
	v_fma_f32 v25, v25, s69, s69
	v_fma_f32 v26, v26, s69, s69
	v_fma_f32 v27, v27, s69, s69
	v_fma_f32 v28, v28, s69, s69
	v_fma_f32 v29, v29, s69, s69
	v_fma_f32 v30, v30, s69, s69
	v_fma_f32 v31, v31, s69, s69
	v_rcp_f32_e32 v24, v24
	v_rcp_f32_e32 v25, v25
	v_rcp_f32_e32 v26, v26
	v_rcp_f32_e32 v27, v27
	v_rcp_f32_e32 v28, v28
	v_rcp_f32_e32 v29, v29
	v_rcp_f32_e32 v30, v30
	v_rcp_f32_e32 v31, v31
	v_mul_f32_e32 v8, v8, v24
	v_mul_f32_e32 v9, v9, v25
	v_mul_f32_e32 v10, v10, v26
	v_mul_f32_e32 v11, v11, v27
	v_mul_f32_e32 v12, v12, v28
	v_mul_f32_e32 v13, v13, v29
	v_mul_f32_e32 v14, v14, v30
	v_mul_f32_e32 v15, v15, v31
	v_med3_f32 v8, v8, s11, v232
	v_med3_f32 v9, v9, s11, v232
	v_med3_f32 v10, v10, s11, v232
	v_med3_f32 v11, v11, s11, v232
	v_med3_f32 v12, v12, s11, v232
	v_med3_f32 v13, v13, s11, v232
	v_med3_f32 v14, v14, s11, v232
	v_med3_f32 v15, v15, s11, v232
	v_mul_f32_e32 v24, 0xbab8aa3b, v110
	v_mul_f32_e32 v25, 0xbab8aa3b, v111
	v_mul_f32_e32 v26, 0xbab8aa3b, v112
	v_mul_f32_e32 v27, 0xbab8aa3b, v113
	v_mul_f32_e32 v28, 0xbab8aa3b, v102
	v_mul_f32_e32 v29, 0xbab8aa3b, v103
	v_mul_f32_e32 v30, 0xbab8aa3b, v104
	v_mul_f32_e32 v31, 0xbab8aa3b, v105
	v_exp_f32_e32 v24, v24
	v_exp_f32_e32 v25, v25
	v_exp_f32_e32 v26, v26
	v_exp_f32_e32 v27, v27
	v_exp_f32_e32 v28, v28
	v_exp_f32_e32 v29, v29
	v_exp_f32_e32 v30, v30
	v_exp_f32_e32 v31, v31
	v_mul_f32_e32 v16, v110, v106
	v_mul_f32_e32 v17, v111, v107
	v_mul_f32_e32 v18, v112, v108
	v_mul_f32_e32 v19, v113, v109
	v_mul_f32_e32 v20, v102, v98
	v_mul_f32_e32 v21, v103, v99
	v_mul_f32_e32 v22, v104, v100
	v_mul_f32_e32 v23, v105, v101
	v_fma_f32 v24, v24, s69, s69
	v_fma_f32 v25, v25, s69, s69
	v_fma_f32 v26, v26, s69, s69
	v_fma_f32 v27, v27, s69, s69
	v_fma_f32 v28, v28, s69, s69
	v_fma_f32 v29, v29, s69, s69
	v_fma_f32 v30, v30, s69, s69
	v_fma_f32 v31, v31, s69, s69
	v_rcp_f32_e32 v24, v24
	v_rcp_f32_e32 v25, v25
	v_rcp_f32_e32 v26, v26
	v_rcp_f32_e32 v27, v27
	v_rcp_f32_e32 v28, v28
	v_rcp_f32_e32 v29, v29
	v_rcp_f32_e32 v30, v30
	v_rcp_f32_e32 v31, v31
	v_mul_f32_e32 v16, v16, v24
	v_mul_f32_e32 v17, v17, v25
	v_mul_f32_e32 v18, v18, v26
	v_mul_f32_e32 v19, v19, v27
	v_mul_f32_e32 v20, v20, v28
	v_mul_f32_e32 v21, v21, v29
	v_mul_f32_e32 v22, v22, v30
	v_mul_f32_e32 v23, v23, v31
	v_med3_f32 v16, v16, s11, v232
	v_med3_f32 v17, v17, s11, v232
	v_med3_f32 v18, v18, s11, v232
	v_med3_f32 v19, v19, s11, v232
	v_med3_f32 v20, v20, s11, v232
	v_med3_f32 v21, v21, s11, v232
	v_med3_f32 v22, v22, s11, v232
	v_med3_f32 v23, v23, s11, v232
	v_cvt_pk_fp8_f32 v0, v8, v9
	v_cvt_pk_fp8_f32 v1, v12, v13
	v_cvt_pk_fp8_f32 v2, v16, v17
	v_cvt_pk_fp8_f32 v3, v20, v21
	v_cvt_pk_fp8_f32 v0, v10, v11 op_sel:[0,0,1]
	v_cvt_pk_fp8_f32 v1, v14, v15 op_sel:[0,0,1]
	v_cvt_pk_fp8_f32 v2, v18, v19 op_sel:[0,0,1]
	v_cvt_pk_fp8_f32 v3, v22, v23 op_sel:[0,0,1]
	v_ashrrev_i32_e32 v7, 31, v6
	v_lshlrev_b64 v[6:7], 10, v[6:7]
	v_lshl_add_u64 v[6:7], s[58:59], 0, v[6:7]
	v_lshl_add_u64 v[6:7], v[6:7], 0, v[48:49]
	s_nop 1
	v_permlane16_swap_b32_e32 v0, v2
	v_permlane16_swap_b32_e32 v1, v3
	global_store_dwordx4 v[6:7], v[0:3], off
	v_mov_b32_e32 v98, 0
	v_mov_b32_e32 v99, 0
	v_mov_b32_e32 v100, 0
	v_mov_b32_e32 v101, 0
	v_mov_b32_e32 v102, 0
	v_mov_b32_e32 v103, 0
	v_mov_b32_e32 v104, 0
	v_mov_b32_e32 v105, 0
	v_mov_b32_e32 v106, 0
	v_mov_b32_e32 v107, 0
	v_mov_b32_e32 v108, 0
	v_mov_b32_e32 v109, 0
	v_mov_b32_e32 v110, 0
	v_mov_b32_e32 v111, 0
	v_mov_b32_e32 v112, 0
	v_mov_b32_e32 v113, 0
	v_mov_b32_e32 v114, 0
	v_mov_b32_e32 v115, 0
	v_mov_b32_e32 v116, 0
	v_mov_b32_e32 v117, 0
	v_mov_b32_e32 v118, 0
	v_mov_b32_e32 v119, 0
	v_mov_b32_e32 v120, 0
	v_mov_b32_e32 v121, 0
	v_mov_b32_e32 v122, 0
	v_mov_b32_e32 v123, 0
	v_mov_b32_e32 v124, 0
	v_mov_b32_e32 v125, 0
	v_mov_b32_e32 v126, 0
	v_mov_b32_e32 v127, 0
	v_mov_b32_e32 v128, 0
	v_mov_b32_e32 v129, 0
	v_mul_f32_e32 v24, 0xbab8aa3b, v94
	v_mul_f32_e32 v25, 0xbab8aa3b, v95
	v_mul_f32_e32 v26, 0xbab8aa3b, v96
	v_mul_f32_e32 v27, 0xbab8aa3b, v97
	v_mul_f32_e32 v28, 0xbab8aa3b, v86
	v_mul_f32_e32 v29, 0xbab8aa3b, v87
	v_mul_f32_e32 v30, 0xbab8aa3b, v88
	v_mul_f32_e32 v31, 0xbab8aa3b, v89
	v_exp_f32_e32 v24, v24
	v_exp_f32_e32 v25, v25
	v_exp_f32_e32 v26, v26
	v_exp_f32_e32 v27, v27
	v_exp_f32_e32 v28, v28
	v_exp_f32_e32 v29, v29
	v_exp_f32_e32 v30, v30
	v_exp_f32_e32 v31, v31
	v_mul_f32_e32 v8, v94, v90
	v_mul_f32_e32 v9, v95, v91
	v_mul_f32_e32 v10, v96, v92
	v_mul_f32_e32 v11, v97, v93
	v_mul_f32_e32 v12, v86, v82
	v_mul_f32_e32 v13, v87, v83
	v_mul_f32_e32 v14, v88, v84
	v_mul_f32_e32 v15, v89, v85
	v_fma_f32 v24, v24, s69, s69
	v_fma_f32 v25, v25, s69, s69
	v_fma_f32 v26, v26, s69, s69
	v_fma_f32 v27, v27, s69, s69
	v_fma_f32 v28, v28, s69, s69
	v_fma_f32 v29, v29, s69, s69
	v_fma_f32 v30, v30, s69, s69
	v_fma_f32 v31, v31, s69, s69
	v_rcp_f32_e32 v24, v24
	v_rcp_f32_e32 v25, v25
	v_rcp_f32_e32 v26, v26
	v_rcp_f32_e32 v27, v27
	v_rcp_f32_e32 v28, v28
	v_rcp_f32_e32 v29, v29
	v_rcp_f32_e32 v30, v30
	v_rcp_f32_e32 v31, v31
	v_mul_f32_e32 v8, v8, v24
	v_mul_f32_e32 v9, v9, v25
	v_mul_f32_e32 v10, v10, v26
	v_mul_f32_e32 v11, v11, v27
	v_mul_f32_e32 v12, v12, v28
	v_mul_f32_e32 v13, v13, v29
	v_mul_f32_e32 v14, v14, v30
	v_mul_f32_e32 v15, v15, v31
	v_med3_f32 v8, v8, s11, v232
	v_med3_f32 v9, v9, s11, v232
	v_med3_f32 v10, v10, s11, v232
	v_med3_f32 v11, v11, s11, v232
	v_med3_f32 v12, v12, s11, v232
	v_med3_f32 v13, v13, s11, v232
	v_med3_f32 v14, v14, s11, v232
	v_med3_f32 v15, v15, s11, v232
	v_mul_f32_e32 v24, 0xbab8aa3b, v78
	v_mul_f32_e32 v25, 0xbab8aa3b, v79
	v_mul_f32_e32 v26, 0xbab8aa3b, v80
	v_mul_f32_e32 v27, 0xbab8aa3b, v81
	v_mul_f32_e32 v28, 0xbab8aa3b, v70
	v_mul_f32_e32 v29, 0xbab8aa3b, v71
	v_mul_f32_e32 v30, 0xbab8aa3b, v72
	v_mul_f32_e32 v31, 0xbab8aa3b, v73
	v_exp_f32_e32 v24, v24
	v_exp_f32_e32 v25, v25
	v_exp_f32_e32 v26, v26
	v_exp_f32_e32 v27, v27
	v_exp_f32_e32 v28, v28
	v_exp_f32_e32 v29, v29
	v_exp_f32_e32 v30, v30
	v_exp_f32_e32 v31, v31
	v_mul_f32_e32 v16, v78, v74
	v_mul_f32_e32 v17, v79, v75
	v_mul_f32_e32 v18, v80, v76
	v_mul_f32_e32 v19, v81, v77
	v_mul_f32_e32 v20, v70, v66
	v_mul_f32_e32 v21, v71, v67
	v_mul_f32_e32 v22, v72, v68
	v_mul_f32_e32 v23, v73, v69
	v_fma_f32 v24, v24, s69, s69
	v_fma_f32 v25, v25, s69, s69
	v_fma_f32 v26, v26, s69, s69
	v_fma_f32 v27, v27, s69, s69
	v_fma_f32 v28, v28, s69, s69
	v_fma_f32 v29, v29, s69, s69
	v_fma_f32 v30, v30, s69, s69
	v_fma_f32 v31, v31, s69, s69
	v_rcp_f32_e32 v24, v24
	v_rcp_f32_e32 v25, v25
	v_rcp_f32_e32 v26, v26
	v_rcp_f32_e32 v27, v27
	v_rcp_f32_e32 v28, v28
	v_rcp_f32_e32 v29, v29
	v_rcp_f32_e32 v30, v30
	v_rcp_f32_e32 v31, v31
	v_mul_f32_e32 v16, v16, v24
	v_mul_f32_e32 v17, v17, v25
	v_mul_f32_e32 v18, v18, v26
	v_mul_f32_e32 v19, v19, v27
	v_mul_f32_e32 v20, v20, v28
	v_mul_f32_e32 v21, v21, v29
	v_mul_f32_e32 v22, v22, v30
	v_mul_f32_e32 v23, v23, v31
	v_med3_f32 v16, v16, s11, v232
	v_med3_f32 v17, v17, s11, v232
	v_med3_f32 v18, v18, s11, v232
	v_med3_f32 v19, v19, s11, v232
	v_med3_f32 v20, v20, s11, v232
	v_med3_f32 v21, v21, s11, v232
	v_med3_f32 v22, v22, s11, v232
	v_med3_f32 v23, v23, s11, v232
	v_cvt_pk_fp8_f32 v0, v8, v9
	v_cvt_pk_fp8_f32 v1, v12, v13
	v_cvt_pk_fp8_f32 v2, v16, v17
	v_cvt_pk_fp8_f32 v3, v20, v21
	v_cvt_pk_fp8_f32 v0, v10, v11 op_sel:[0,0,1]
	v_cvt_pk_fp8_f32 v1, v14, v15 op_sel:[0,0,1]
	v_cvt_pk_fp8_f32 v2, v18, v19 op_sel:[0,0,1]
	v_cvt_pk_fp8_f32 v3, v22, v23 op_sel:[0,0,1]
	v_add_co_u32_e32 v6, vcc, s0, v4
	s_nop 1
	v_addc_co_u32_e32 v7, vcc, 0, v5, vcc
	s_nop 1
	v_permlane16_swap_b32_e32 v0, v2
	v_permlane16_swap_b32_e32 v1, v3
	global_store_dwordx4 v[6:7], v[0:3], off
	v_mov_b32_e32 v66, 0
	v_mov_b32_e32 v67, 0
	v_mov_b32_e32 v68, 0
	v_mov_b32_e32 v69, 0
	v_mov_b32_e32 v70, 0
	v_mov_b32_e32 v71, 0
	v_mov_b32_e32 v72, 0
	v_mov_b32_e32 v73, 0
	v_mov_b32_e32 v74, 0
	v_mov_b32_e32 v75, 0
	v_mov_b32_e32 v76, 0
	v_mov_b32_e32 v77, 0
	v_mov_b32_e32 v78, 0
	v_mov_b32_e32 v79, 0
	v_mov_b32_e32 v80, 0
	v_mov_b32_e32 v81, 0
	v_mov_b32_e32 v82, 0
	v_mov_b32_e32 v83, 0
	v_mov_b32_e32 v84, 0
	v_mov_b32_e32 v85, 0
	v_mov_b32_e32 v86, 0
	v_mov_b32_e32 v87, 0
	v_mov_b32_e32 v88, 0
	v_mov_b32_e32 v89, 0
	v_mov_b32_e32 v90, 0
	v_mov_b32_e32 v91, 0
	v_mov_b32_e32 v92, 0
	v_mov_b32_e32 v93, 0
	v_mov_b32_e32 v94, 0
	v_mov_b32_e32 v95, 0
	v_mov_b32_e32 v96, 0
	v_mov_b32_e32 v97, 0
	v_mul_f32_e32 v24, 0xbab8aa3b, v62
	v_mul_f32_e32 v25, 0xbab8aa3b, v63
	v_mul_f32_e32 v26, 0xbab8aa3b, v64
	v_mul_f32_e32 v27, 0xbab8aa3b, v65
	v_mul_f32_e32 v28, 0xbab8aa3b, v54
	v_mul_f32_e32 v29, 0xbab8aa3b, v55
	v_mul_f32_e32 v30, 0xbab8aa3b, v56
	v_mul_f32_e32 v31, 0xbab8aa3b, v57
	v_exp_f32_e32 v24, v24
	v_exp_f32_e32 v25, v25
	v_exp_f32_e32 v26, v26
	v_exp_f32_e32 v27, v27
	v_exp_f32_e32 v28, v28
	v_exp_f32_e32 v29, v29
	v_exp_f32_e32 v30, v30
	v_exp_f32_e32 v31, v31
	v_mul_f32_e32 v8, v62, v58
	v_mul_f32_e32 v9, v63, v59
	v_mul_f32_e32 v10, v64, v60
	v_mul_f32_e32 v11, v65, v61
	v_mul_f32_e32 v12, v54, v50
	v_mul_f32_e32 v13, v55, v51
	v_mul_f32_e32 v14, v56, v52
	v_mul_f32_e32 v15, v57, v53
	v_fma_f32 v24, v24, s69, s69
	v_fma_f32 v25, v25, s69, s69
	v_fma_f32 v26, v26, s69, s69
	v_fma_f32 v27, v27, s69, s69
	v_fma_f32 v28, v28, s69, s69
	v_fma_f32 v29, v29, s69, s69
	v_fma_f32 v30, v30, s69, s69
	v_fma_f32 v31, v31, s69, s69
	v_rcp_f32_e32 v24, v24
	v_rcp_f32_e32 v25, v25
	v_rcp_f32_e32 v26, v26
	v_rcp_f32_e32 v27, v27
	v_rcp_f32_e32 v28, v28
	v_rcp_f32_e32 v29, v29
	v_rcp_f32_e32 v30, v30
	v_rcp_f32_e32 v31, v31
	v_mul_f32_e32 v8, v8, v24
	v_mul_f32_e32 v9, v9, v25
	v_mul_f32_e32 v10, v10, v26
	v_mul_f32_e32 v11, v11, v27
	v_mul_f32_e32 v12, v12, v28
	v_mul_f32_e32 v13, v13, v29
	v_mul_f32_e32 v14, v14, v30
	v_mul_f32_e32 v15, v15, v31
	v_med3_f32 v8, v8, s11, v232
	v_med3_f32 v9, v9, s11, v232
	v_med3_f32 v10, v10, s11, v232
	v_med3_f32 v11, v11, s11, v232
	v_med3_f32 v12, v12, s11, v232
	v_med3_f32 v13, v13, s11, v232
	v_med3_f32 v14, v14, s11, v232
	v_med3_f32 v15, v15, s11, v232
	v_mul_f32_e32 v24, 0xbab8aa3b, v44
	v_mul_f32_e32 v25, 0xbab8aa3b, v45
	v_mul_f32_e32 v26, 0xbab8aa3b, v46
	v_mul_f32_e32 v27, 0xbab8aa3b, v47
	v_mul_f32_e32 v28, 0xbab8aa3b, v36
	v_mul_f32_e32 v29, 0xbab8aa3b, v37
	v_mul_f32_e32 v30, 0xbab8aa3b, v38
	v_mul_f32_e32 v31, 0xbab8aa3b, v39
	v_exp_f32_e32 v24, v24
	v_exp_f32_e32 v25, v25
	v_exp_f32_e32 v26, v26
	v_exp_f32_e32 v27, v27
	v_exp_f32_e32 v28, v28
	v_exp_f32_e32 v29, v29
	v_exp_f32_e32 v30, v30
	v_exp_f32_e32 v31, v31
	v_mul_f32_e32 v16, v44, v40
	v_mul_f32_e32 v17, v45, v41
	v_mul_f32_e32 v18, v46, v42
	v_mul_f32_e32 v19, v47, v43
	v_mul_f32_e32 v20, v36, v32
	v_mul_f32_e32 v21, v37, v33
	v_mul_f32_e32 v22, v38, v34
	v_mul_f32_e32 v23, v39, v35
	v_fma_f32 v24, v24, s69, s69
	v_fma_f32 v25, v25, s69, s69
	v_fma_f32 v26, v26, s69, s69
	v_fma_f32 v27, v27, s69, s69
	v_fma_f32 v28, v28, s69, s69
	v_fma_f32 v29, v29, s69, s69
	v_fma_f32 v30, v30, s69, s69
	v_fma_f32 v31, v31, s69, s69
	v_rcp_f32_e32 v24, v24
	v_rcp_f32_e32 v25, v25
	v_rcp_f32_e32 v26, v26
	v_rcp_f32_e32 v27, v27
	v_rcp_f32_e32 v28, v28
	v_rcp_f32_e32 v29, v29
	v_rcp_f32_e32 v30, v30
	v_rcp_f32_e32 v31, v31
	v_mul_f32_e32 v16, v16, v24
	v_mul_f32_e32 v17, v17, v25
	v_mul_f32_e32 v18, v18, v26
	v_mul_f32_e32 v19, v19, v27
	v_mul_f32_e32 v20, v20, v28
	v_mul_f32_e32 v21, v21, v29
	v_mul_f32_e32 v22, v22, v30
	v_mul_f32_e32 v23, v23, v31
	v_med3_f32 v16, v16, s11, v232
	v_med3_f32 v17, v17, s11, v232
	v_med3_f32 v18, v18, s11, v232
	v_med3_f32 v19, v19, s11, v232
	v_med3_f32 v20, v20, s11, v232
	v_med3_f32 v21, v21, s11, v232
	v_med3_f32 v22, v22, s11, v232
	v_med3_f32 v23, v23, s11, v232
	v_cvt_pk_fp8_f32 v0, v8, v9
	v_cvt_pk_fp8_f32 v1, v12, v13
	v_cvt_pk_fp8_f32 v2, v16, v17
	v_cvt_pk_fp8_f32 v3, v20, v21
	v_cvt_pk_fp8_f32 v0, v10, v11 op_sel:[0,0,1]
	v_cvt_pk_fp8_f32 v1, v14, v15 op_sel:[0,0,1]
	v_cvt_pk_fp8_f32 v2, v18, v19 op_sel:[0,0,1]
	v_cvt_pk_fp8_f32 v3, v22, v23 op_sel:[0,0,1]
	v_add_co_u32_e32 v4, vcc, 0x28000, v4
	s_nop 1
	v_addc_co_u32_e32 v5, vcc, 0, v5, vcc
	s_mov_b64 s[0:1], -1
	s_nop 1
	v_permlane16_swap_b32_e32 v0, v2
	v_permlane16_swap_b32_e32 v1, v3
	s_andn2_b64 vcc, exec, s[38:39]
	global_store_dwordx4 v[4:5], v[0:3], off
	v_mov_b32_e32 v32, 0
	v_mov_b32_e32 v33, 0
	v_mov_b32_e32 v34, 0
	v_mov_b32_e32 v35, 0
	v_mov_b32_e32 v36, 0
	v_mov_b32_e32 v37, 0
	v_mov_b32_e32 v38, 0
	v_mov_b32_e32 v39, 0
	v_mov_b32_e32 v40, 0
	v_mov_b32_e32 v41, 0
	v_mov_b32_e32 v42, 0
	v_mov_b32_e32 v43, 0
	v_mov_b32_e32 v44, 0
	v_mov_b32_e32 v45, 0
	v_mov_b32_e32 v46, 0
	v_mov_b32_e32 v47, 0
	v_mov_b32_e32 v50, 0
	v_mov_b32_e32 v51, 0
	v_mov_b32_e32 v52, 0
	v_mov_b32_e32 v53, 0
	v_mov_b32_e32 v54, 0
	v_mov_b32_e32 v55, 0
	v_mov_b32_e32 v56, 0
	v_mov_b32_e32 v57, 0
	v_mov_b32_e32 v58, 0
	v_mov_b32_e32 v59, 0
	v_mov_b32_e32 v60, 0
	v_mov_b32_e32 v61, 0
	v_mov_b32_e32 v62, 0
	v_mov_b32_e32 v63, 0
	v_mov_b32_e32 v64, 0
	v_mov_b32_e32 v65, 0
	s_cbranch_vccnz .LBB0_849
	s_andn2_b64 vcc, exec, s[56:57]
	s_cbranch_vccnz .LBB0_848
	s_barrier
	s_branch .LBB0_848
